# lru unit: scan rows read with immediate offsets in forward and backward copies; output store addresses advance by a per-wave stride
# speedup vs baseline: 1.0012x; 1.0006x over previous
.LBB0_370:
	v_ashrrev_i32_e32 v11, 6, v30
	v_add_u32_e32 v8, v111, v104
	s_waitcnt lgkmcnt(0)
	s_barrier
	v_lshl_add_u32 v22, v11, 8, v8
	ds_read2st64_b32 v[112:113], v22 offset1:1
	ds_read2st64_b32 v[114:115], v22 offset0:2 offset1:3
	ds_read2st64_b32 v[116:117], v22 offset0:8 offset1:9
	ds_read2st64_b32 v[118:119], v22 offset0:10 offset1:11
	ds_read2st64_b32 v[120:121], v22 offset0:16 offset1:17
	ds_read2st64_b32 v[122:123], v22 offset0:18 offset1:19
	ds_read2st64_b32 v[124:125], v22 offset0:24 offset1:25
	ds_read2st64_b32 v[126:127], v22 offset0:26 offset1:27
	ds_read2st64_b32 v[128:129], v22 offset0:32 offset1:33
	ds_read2st64_b32 v[130:131], v22 offset0:34 offset1:35
	ds_read2st64_b32 v[132:133], v22 offset0:40 offset1:41
	ds_read2st64_b32 v[134:135], v22 offset0:42 offset1:43
	ds_read2st64_b32 v[136:137], v22 offset0:48 offset1:49
	ds_read2st64_b32 v[138:139], v22 offset0:50 offset1:51
	ds_read2st64_b32 v[140:141], v22 offset0:56 offset1:57
	ds_read2st64_b32 v[142:143], v22 offset0:58 offset1:59
	v_lshlrev_b32_e32 v9, 1, v31
	s_movk_i32 s0, 0x104
	v_sub_u32_e32 v10, v8, v9
	v_mad_u64_u32 v[8:9], s[0:1], v11, s0, v[8:9]
	s_waitcnt vmcnt(12) lgkmcnt(0)
	v_fma_f32 v23, v15, v112, v14
	v_fmac_f32_e32 v23, v21, v113
	v_mad_u64_u32 v[10:11], s[0:1], v11, s39, v[10:11]
	s_or_b32 s0, s24, s71
	s_ashr_i32 s1, s0, 31
	v_fmac_f32_e32 v23, v12, v114
	v_fmac_f32_e32 v23, v13, v115
	ds_write_b32 v8, v23 offset:17408
	v_bfe_u32 v9, v23, 16, 1
	v_add3_u32 v9, v23, v9, s25
	ds_write_b16_d16_hi v10, v9 offset:34304
	s_lshl_b64 s[0:1], s[0:1], 13
	v_fma_f32 v9, v15, v116, v14
	v_fmac_f32_e32 v9, v21, v117
	s_add_u32 s2, s69, s0
	s_addc_u32 s3, s70, s1
	v_and_b32_e32 v24, 48, v30
	v_mov_b32_e32 v25, v105
	v_fmac_f32_e32 v9, v12, v118
	v_fmac_f32_e32 v9, v13, v119
	ds_write_b32 v8, v9 offset:19488
	v_bfe_u32 v11, v9, 16, 1
	v_add3_u32 v9, v9, v11, s25
	ds_write_b16_d16_hi v10, v9 offset:35456
	s_or_b32 s0, s24, s72
	v_fma_f32 v9, v15, v120, v14
	v_fmac_f32_e32 v9, v21, v121
	s_ashr_i32 s1, s0, 31
	s_lshl_b64 s[0:1], s[0:1], 13
	s_add_u32 s0, s69, s0
	s_addc_u32 s1, s70, s1
	v_fmac_f32_e32 v9, v12, v122
	v_fmac_f32_e32 v9, v13, v123
	ds_write_b32 v8, v9 offset:21568
	v_bfe_u32 v11, v9, 16, 1
	v_add3_u32 v9, v9, v11, s25
	ds_write_b16_d16_hi v10, v9 offset:36608
	s_mov_b32 s14, 0xbfb8aa3b
	v_fma_f32 v9, v15, v124, v14
	v_fmac_f32_e32 v9, v21, v125
	v_or_b32_e32 v47, 16, v35
	v_cmp_gt_u32_e32 vcc, s21, v30
	v_mov_b32_e32 v67, 1.0
	v_mov_b32_e32 v68, 0
	v_fmac_f32_e32 v9, v12, v126
	v_fmac_f32_e32 v9, v13, v127
	ds_write_b32 v8, v9 offset:23648
	v_bfe_u32 v11, v9, 16, 1
	v_add3_u32 v9, v9, v11, s25
	ds_write_b16_d16_hi v10, v9 offset:37760
	v_fma_f32 v9, v15, v128, v14
	v_fmac_f32_e32 v9, v21, v129
	v_fmac_f32_e32 v9, v12, v130
	v_fmac_f32_e32 v9, v13, v131
	ds_write_b32 v8, v9 offset:25728
	v_bfe_u32 v11, v9, 16, 1
	v_add3_u32 v9, v9, v11, s25
	ds_write_b16_d16_hi v10, v9 offset:38912
	v_fma_f32 v9, v15, v132, v14
	v_fmac_f32_e32 v9, v21, v133
	v_fmac_f32_e32 v9, v12, v134
	v_fmac_f32_e32 v9, v13, v135
	ds_write_b32 v8, v9 offset:27808
	v_bfe_u32 v11, v9, 16, 1
	v_add3_u32 v9, v9, v11, s25
	ds_write_b16_d16_hi v10, v9 offset:40064
	v_fma_f32 v9, v15, v136, v14
	v_fmac_f32_e32 v9, v21, v137
	v_fmac_f32_e32 v9, v12, v138
	v_fmac_f32_e32 v9, v13, v139
	ds_write_b32 v8, v9 offset:29888
	v_bfe_u32 v11, v9, 16, 1
	v_add3_u32 v9, v9, v11, s25
	ds_write_b16_d16_hi v10, v9 offset:41216
	v_fmac_f32_e32 v14, v15, v140
	v_fmac_f32_e32 v14, v21, v141
	v_fmac_f32_e32 v14, v12, v142
	v_fmac_f32_e32 v14, v13, v143
	ds_write_b32 v8, v14 offset:31968
	v_bfe_u32 v8, v14, 16, 1
	v_add3_u32 v8, v14, v8, s25
	v_lshrrev_b32_e32 v16, 2, v30
	ds_write_b16_d16_hi v10, v8 offset:42368
	v_or_b32_e32 v8, s34, v35
	v_and_or_b32 v21, v16, 12, s34
	v_lshlrev_b32_e32 v16, 7, v35
	v_mov_b32_e32 v17, v105
	v_mul_u32_u24_e32 v8, 0x90, v8
	v_lshl_add_u64 v[22:23], s[2:3], 0, v[16:17]
	s_waitcnt lgkmcnt(0)
	s_barrier
	v_add3_u32 v8, v111, v8, v24
	v_lshl_add_u64 v[22:23], v[22:23], 0, v[24:25]
	ds_read_b128 v[12:15], v8 offset:34304
	ds_read_b128 v[8:11], v8 offset:34368
	global_load_dwordx4 v[36:39], v[22:23], off
	global_load_dwordx4 v[48:51], v[22:23], off offset:64
	v_lshl_add_u64 v[16:17], s[0:1], 0, v[16:17]
	v_lshl_add_u64 v[16:17], v[16:17], 0, v[24:25]
	v_lshlrev_b32_e32 v42, 6, v21
	s_waitcnt vmcnt(1) lgkmcnt(1)
	v_mfma_f32_16x16x32_bf16 v[36:39], v[12:15], v[36:39], 0
	global_load_dwordx4 v[52:55], v[16:17], off offset:64
	s_waitcnt vmcnt(1) lgkmcnt(0)
	v_mfma_f32_16x16x32_bf16 v[48:51], v[8:11], v[48:51], v[36:39]
	s_nop 4
	global_load_dwordx4 v[36:39], v[16:17], off
	v_mul_f32_e64 v17, |v20|, s14
	s_nop 0
	v_add_f32_e32 v22, v18, v48
	v_mul_f32_e32 v22, 0xbfb8aa3b, v22
	v_exp_f32_e32 v17, v17
	v_exp_f32_e32 v22, v22
	v_max_f32_e64 v16, -v20, -v20
	v_max_f32_e32 v16, 0, v16
	v_add_f32_e32 v17, 1.0, v17
	v_add_f32_e32 v22, 1.0, v22
	v_log_f32_e32 v17, v17
	v_rcp_f32_e32 v22, v22
	v_or_b32_e32 v20, s73, v35
	v_lshlrev_b32_e32 v48, 7, v47
	v_fmac_f32_e32 v16, 0x3f317218, v17
	v_mul_f32_e32 v22, 0xc1000000, v22
	v_mul_f32_e32 v22, v16, v22
	v_mul_f32_e32 v22, 0x3fb8aa3b, v22
	v_exp_f32_e32 v22, v22
	v_lshlrev_b32_e32 v17, 2, v35
	s_waitcnt vmcnt(0)
	v_mfma_f32_16x16x32_bf16 v[36:39], v[12:15], v[36:39], 0
	v_mfma_f32_16x16x32_bf16 v[52:55], v[8:11], v[52:55], v[36:39]
	s_nop 6
	v_fma_f32 v36, -v22, v22, 1.0
	v_max_f32_e32 v36, 0, v36
	v_add_f32_e32 v23, v19, v52
	v_mul_f32_e32 v23, 0xbfb8aa3b, v23
	v_exp_f32_e32 v23, v23
	v_sqrt_f32_e32 v36, v36
	v_or_b32_e32 v39, 64, v42
	v_or_b32_e32 v38, 0x80, v42
	v_add_f32_e32 v23, 1.0, v23
	v_rcp_f32_e32 v23, v23
	v_or_b32_e32 v37, 0xc0, v42
	v_mul_f32_e32 v23, v23, v36
	v_mul_u32_u24_e32 v36, 0x104, v21
	v_add3_u32 v36, v111, v17, v36
	ds_read_b32 v144, v36 offset:17408
	ds_read_b32 v145, v36 offset:17668
	ds_read_b32 v146, v36 offset:17928
	ds_read_b32 v147, v36 offset:18188
	ds_read_b32 v148, v36 offset:17472
	ds_read_b32 v149, v36 offset:17732
	ds_read_b32 v150, v36 offset:17992
	ds_read_b32 v151, v36 offset:18252
	ds_read_b32 v152, v36 offset:17536
	ds_read_b32 v153, v36 offset:17796
	ds_read_b32 v154, v36 offset:18056
	ds_read_b32 v155, v36 offset:18316
	ds_read_b32 v156, v36 offset:17600
	ds_read_b32 v157, v36 offset:17860
	ds_read_b32 v158, v36 offset:18120
	ds_read_b32 v159, v36 offset:18380
	v_or_b32_e32 v21, v42, v20
	v_lshlrev_b32_e32 v21, 2, v21
	s_waitcnt lgkmcnt(0)
	v_mul_f32_e32 v17, v144, v23
	v_add_u32_e32 v23, v111, v21
	v_add_u32_e32 v21, v28, v21
	ds_write_b32 v23, v22 offset:43520
	ds_write_b32 v21, v17
	v_add_f32_e32 v17, v18, v49
	v_mul_f32_e32 v17, 0xbfb8aa3b, v17
	v_exp_f32_e32 v17, v17
	v_add_f32_e32 v21, v19, v53
	v_mul_f32_e32 v21, 0xbfb8aa3b, v21
	v_exp_f32_e32 v21, v21
	v_add_f32_e32 v17, 1.0, v17
	v_rcp_f32_e32 v17, v17
	v_mov_b32_e32 v49, v105
	v_add_f32_e32 v21, 1.0, v21
	v_rcp_f32_e32 v21, v21
	v_mul_f32_e32 v17, 0xc1000000, v17
	v_mul_f32_e32 v17, v16, v17
	v_mul_f32_e32 v17, 0x3fb8aa3b, v17
	v_exp_f32_e32 v17, v17
	s_nop 0
	v_fma_f32 v22, -v17, v17, 1.0
	v_max_f32_e32 v22, 0, v22
	v_sqrt_f32_e32 v22, v22
	s_nop 0
	v_mul_f32_e32 v21, v21, v22
	v_mul_f32_e32 v21, v145, v21
	v_or_b32_e32 v22, v39, v20
	v_lshlrev_b32_e32 v22, 2, v22
	v_add_u32_e32 v23, v111, v22
	ds_write_b32 v23, v17 offset:43520
	v_add_u32_e32 v17, v28, v22
	ds_write_b32 v17, v21
	v_add_f32_e32 v17, v18, v50
	v_mul_f32_e32 v17, 0xbfb8aa3b, v17
	v_exp_f32_e32 v17, v17
	v_add_f32_e32 v21, v19, v54
	v_mul_f32_e32 v21, 0xbfb8aa3b, v21
	v_exp_f32_e32 v21, v21
	v_add_f32_e32 v17, 1.0, v17
	v_rcp_f32_e32 v17, v17
	v_add_f32_e32 v21, 1.0, v21
	v_rcp_f32_e32 v21, v21
	v_mul_f32_e32 v17, 0xc1000000, v17
	v_mul_f32_e32 v17, v16, v17
	v_mul_f32_e32 v17, 0x3fb8aa3b, v17
	v_exp_f32_e32 v17, v17
	s_nop 0
	v_fma_f32 v22, -v17, v17, 1.0
	v_max_f32_e32 v22, 0, v22
	v_sqrt_f32_e32 v22, v22
	s_nop 0
	v_mul_f32_e32 v21, v21, v22
	v_mul_f32_e32 v21, v146, v21
	v_or_b32_e32 v22, v38, v20
	v_lshlrev_b32_e32 v22, 2, v22
	v_add_u32_e32 v23, v111, v22
	ds_write_b32 v23, v17 offset:43520
	v_add_u32_e32 v17, v28, v22
	ds_write_b32 v17, v21
	v_add_f32_e32 v17, v18, v51
	v_mul_f32_e32 v17, 0xbfb8aa3b, v17
	v_exp_f32_e32 v17, v17
	v_add_f32_e32 v18, v19, v55
	v_mul_f32_e32 v18, 0xbfb8aa3b, v18
	v_exp_f32_e32 v18, v18
	v_add_f32_e32 v17, 1.0, v17
	v_rcp_f32_e32 v17, v17
	v_add_f32_e32 v18, 1.0, v18
	v_rcp_f32_e32 v18, v18
	v_mul_f32_e32 v17, 0xc1000000, v17
	v_mul_f32_e32 v16, v16, v17
	v_mul_f32_e32 v16, 0x3fb8aa3b, v16
	v_exp_f32_e32 v16, v16
	s_nop 0
	v_fma_f32 v17, -v16, v16, 1.0
	v_max_f32_e32 v17, 0, v17
	v_sqrt_f32_e32 v17, v17
	s_nop 0
	v_mul_f32_e32 v17, v18, v17
	v_mul_f32_e32 v17, v147, v17
	v_or_b32_e32 v18, v37, v20
	v_lshlrev_b32_e32 v18, 2, v18
	v_add_u32_e32 v19, v111, v18
	ds_write_b32 v19, v16 offset:43520
	v_add_u32_e32 v16, v28, v18
	ds_write_b32 v16, v17
	v_lshl_add_u64 v[16:17], s[2:3], 0, v[48:49]
	v_lshl_add_u64 v[20:21], v[16:17], 0, v[24:25]
	global_load_dwordx4 v[16:19], v[20:21], off
	s_waitcnt vmcnt(0)
	v_mfma_f32_16x16x32_bf16 v[16:19], v[12:15], v[16:19], 0
	global_load_dwordx4 v[20:23], v[20:21], off offset:64
	s_waitcnt vmcnt(0)
	v_mfma_f32_16x16x32_bf16 v[16:19], v[8:11], v[20:23], v[16:19]
	v_lshl_add_u64 v[20:21], s[0:1], 0, v[48:49]
	v_lshl_add_u64 v[48:49], v[20:21], 0, v[24:25]
	global_load_dwordx4 v[20:23], v[48:49], off
	s_waitcnt vmcnt(0)
	v_mfma_f32_16x16x32_bf16 v[20:23], v[12:15], v[20:23], 0
	global_load_dwordx4 v[48:51], v[48:49], off offset:64
	s_nop 1
	v_add_f32_e32 v16, v45, v16
	v_mul_f32_e32 v16, 0xbfb8aa3b, v16
	s_waitcnt vmcnt(0)
	v_mfma_f32_16x16x32_bf16 v[20:23], v[8:11], v[48:51], v[20:23]
	v_max_f32_e64 v48, -v46, -v46
	v_mul_f32_e64 v46, |v46|, s14
	v_exp_f32_e32 v46, v46
	v_exp_f32_e32 v16, v16
	v_max_f32_e32 v49, 0, v48
	s_nop 2
	v_add_f32_e32 v20, v44, v20
	v_add_f32_e32 v46, 1.0, v46
	v_add_f32_e32 v16, 1.0, v16
	v_log_f32_e32 v46, v46
	v_rcp_f32_e32 v16, v16
	v_mul_f32_e32 v20, 0xbfb8aa3b, v20
	v_exp_f32_e32 v20, v20
	v_fmac_f32_e32 v49, 0x3f317218, v46
	v_mul_f32_e32 v16, 0xc1000000, v16
	v_mul_f32_e32 v16, v49, v16
	v_mul_f32_e32 v16, 0x3fb8aa3b, v16
	v_exp_f32_e32 v16, v16
	v_add_f32_e32 v20, 1.0, v20
	v_rcp_f32_e32 v20, v20
	v_add_u32_e32 v51, s73, v35
	v_fma_f32 v46, -v16, v16, 1.0
	v_max_f32_e32 v46, 0, v46
	v_sqrt_f32_e32 v46, v46
	v_or_b32_e32 v50, s73, v47
	v_add_u32_e32 v47, v42, v51
	v_lshl_add_u32 v48, v47, 2, v111
	v_mul_f32_e32 v20, v20, v46
	ds_write_b32 v48, v16 offset:43584
	v_mul_f32_e32 v20, v148, v20
	v_or_b32_e32 v46, v42, v50
	v_lshl_add_u32 v16, v46, 2, v28
	ds_write_b32 v16, v20
	v_add_f32_e32 v16, v45, v17
	v_mul_f32_e32 v16, 0xbfb8aa3b, v16
	v_exp_f32_e32 v16, v16
	v_add_f32_e32 v17, v44, v21
	v_mul_f32_e32 v17, 0xbfb8aa3b, v17
	v_exp_f32_e32 v17, v17
	v_add_f32_e32 v16, 1.0, v16
	v_rcp_f32_e32 v16, v16
	v_add_u32_e32 v21, v39, v51
	v_add_f32_e32 v17, 1.0, v17
	v_rcp_f32_e32 v17, v17
	v_mul_f32_e32 v16, 0xc1000000, v16
	v_mul_f32_e32 v16, v49, v16
	v_mul_f32_e32 v16, 0x3fb8aa3b, v16
	v_exp_f32_e32 v16, v16
	v_lshl_add_u32 v47, v21, 2, v111
	v_fma_f32 v20, -v16, v16, 1.0
	v_max_f32_e32 v20, 0, v20
	v_sqrt_f32_e32 v20, v20
	s_nop 0
	v_mul_f32_e32 v17, v17, v20
	ds_write_b32 v47, v16 offset:43584
	v_mul_f32_e32 v17, v149, v17
	v_or_b32_e32 v20, v39, v50
	v_lshl_add_u32 v16, v20, 2, v28
	ds_write_b32 v16, v17
	v_add_f32_e32 v16, v45, v18
	v_mul_f32_e32 v16, 0xbfb8aa3b, v16
	v_exp_f32_e32 v16, v16
	v_add_f32_e32 v17, v44, v22
	v_mul_f32_e32 v17, 0xbfb8aa3b, v17
	v_exp_f32_e32 v17, v17
	v_add_f32_e32 v16, 1.0, v16
	v_rcp_f32_e32 v16, v16
	v_add_u32_e32 v20, v38, v51
	v_add_f32_e32 v17, 1.0, v17
	v_rcp_f32_e32 v17, v17
	v_mul_f32_e32 v16, 0xc1000000, v16
	v_mul_f32_e32 v16, v49, v16
	v_mul_f32_e32 v16, 0x3fb8aa3b, v16
	v_exp_f32_e32 v16, v16
	v_lshl_add_u32 v46, v20, 2, v111
	v_fma_f32 v18, -v16, v16, 1.0
	v_max_f32_e32 v18, 0, v18
	v_sqrt_f32_e32 v18, v18
	s_nop 0
	v_mul_f32_e32 v17, v17, v18
	ds_write_b32 v46, v16 offset:43584
	v_mul_f32_e32 v17, v150, v17
	v_or_b32_e32 v18, v38, v50
	v_lshl_add_u32 v16, v18, 2, v28
	ds_write_b32 v16, v17
	v_add_f32_e32 v16, v45, v19
	v_mul_f32_e32 v16, 0xbfb8aa3b, v16
	v_exp_f32_e32 v16, v16
	v_add_f32_e32 v17, v44, v23
	v_mul_f32_e32 v17, 0xbfb8aa3b, v17
	v_exp_f32_e32 v17, v17
	v_add_f32_e32 v16, 1.0, v16
	v_rcp_f32_e32 v16, v16
	v_add_u32_e32 v19, v37, v51
	v_add_f32_e32 v17, 1.0, v17
	v_rcp_f32_e32 v17, v17
	v_mul_f32_e32 v16, 0xc1000000, v16
	v_mul_f32_e32 v16, v49, v16
	v_mul_f32_e32 v16, 0x3fb8aa3b, v16
	v_exp_f32_e32 v16, v16
	v_lshl_add_u32 v44, v19, 2, v111
	v_or_b32_e32 v45, 32, v35
	v_mov_b32_e32 v51, v105
	v_fma_f32 v18, -v16, v16, 1.0
	v_max_f32_e32 v18, 0, v18
	v_sqrt_f32_e32 v18, v18
	v_max_f32_e64 v49, -v43, -v43
	v_mul_f32_e64 v43, |v43|, s14
	v_exp_f32_e32 v43, v43
	v_mul_f32_e32 v17, v17, v18
	ds_write_b32 v44, v16 offset:43584
	v_add_f32_e32 v43, 1.0, v43
	v_log_f32_e32 v43, v43
	v_max_f32_e32 v49, 0, v49
	v_mul_f32_e32 v17, v151, v17
	v_or_b32_e32 v18, v37, v50
	v_lshl_add_u32 v16, v18, 2, v28
	v_lshlrev_b32_e32 v50, 7, v45
	ds_write_b32 v16, v17
	v_lshl_add_u64 v[16:17], s[2:3], 0, v[50:51]
	v_lshl_add_u64 v[20:21], v[16:17], 0, v[24:25]
	global_load_dwordx4 v[16:19], v[20:21], off
	s_waitcnt vmcnt(0)
	v_mfma_f32_16x16x32_bf16 v[16:19], v[12:15], v[16:19], 0
	global_load_dwordx4 v[20:23], v[20:21], off offset:64
	v_fmac_f32_e32 v49, 0x3f317218, v43
	v_or_b32_e32 v43, s73, v45
	s_waitcnt vmcnt(0)
	v_mfma_f32_16x16x32_bf16 v[16:19], v[8:11], v[20:23], v[16:19]
	v_lshl_add_u64 v[20:21], s[0:1], 0, v[50:51]
	v_lshl_add_u64 v[50:51], v[20:21], 0, v[24:25]
	global_load_dwordx4 v[20:23], v[50:51], off
	s_nop 4
	v_add_f32_e32 v16, v41, v16
	global_load_dwordx4 v[50:53], v[50:51], off offset:64
	v_mul_f32_e32 v16, 0xbfb8aa3b, v16
	v_exp_f32_e32 v16, v16
	s_waitcnt vmcnt(1)
	v_mfma_f32_16x16x32_bf16 v[20:23], v[12:15], v[20:23], 0
	v_add_f32_e32 v16, 1.0, v16
	v_rcp_f32_e32 v16, v16
	v_or_b32_e32 v35, 48, v35
	s_waitcnt vmcnt(0)
	v_mfma_f32_16x16x32_bf16 v[20:23], v[8:11], v[50:53], v[20:23]
	v_mul_f32_e32 v16, 0xc1000000, v16
	v_mul_f32_e32 v16, v49, v16
	v_mul_f32_e32 v16, 0x3fb8aa3b, v16
	v_exp_f32_e32 v16, v16
	s_nop 3
	v_add_f32_e32 v20, v40, v20
	v_mul_f32_e32 v20, 0xbfb8aa3b, v20
	v_exp_f32_e32 v20, v20
	v_fma_f32 v45, -v16, v16, 1.0
	v_max_f32_e32 v45, 0, v45
	v_sqrt_f32_e32 v45, v45
	v_add_f32_e32 v20, 1.0, v20
	v_rcp_f32_e32 v20, v20
	s_nop 0
	v_mul_f32_e32 v20, v20, v45
	ds_write_b32 v48, v16 offset:43648
	v_mul_f32_e32 v20, v152, v20
	v_or_b32_e32 v45, v42, v43
	v_lshl_add_u32 v16, v45, 2, v28
	ds_write_b32 v16, v20
	v_add_f32_e32 v16, v41, v17
	v_mul_f32_e32 v16, 0xbfb8aa3b, v16
	v_exp_f32_e32 v16, v16
	v_add_f32_e32 v17, v40, v21
	v_mul_f32_e32 v17, 0xbfb8aa3b, v17
	v_exp_f32_e32 v17, v17
	v_add_f32_e32 v16, 1.0, v16
	v_rcp_f32_e32 v16, v16
	v_add_f32_e32 v17, 1.0, v17
	v_rcp_f32_e32 v17, v17
	v_mul_f32_e32 v16, 0xc1000000, v16
	v_mul_f32_e32 v16, v49, v16
	v_mul_f32_e32 v16, 0x3fb8aa3b, v16
	v_exp_f32_e32 v16, v16
	s_nop 0
	v_fma_f32 v20, -v16, v16, 1.0
	v_max_f32_e32 v20, 0, v20
	v_sqrt_f32_e32 v20, v20
	s_nop 0
	v_mul_f32_e32 v17, v17, v20
	ds_write_b32 v47, v16 offset:43648
	v_mul_f32_e32 v17, v153, v17
	v_or_b32_e32 v20, v39, v43
	v_lshl_add_u32 v16, v20, 2, v28
	ds_write_b32 v16, v17
	v_add_f32_e32 v16, v41, v18
	v_mul_f32_e32 v16, 0xbfb8aa3b, v16
	v_exp_f32_e32 v16, v16
	v_add_f32_e32 v17, v40, v22
	v_mul_f32_e32 v17, 0xbfb8aa3b, v17
	v_exp_f32_e32 v17, v17
	v_add_f32_e32 v16, 1.0, v16
	v_rcp_f32_e32 v16, v16
	v_add_f32_e32 v17, 1.0, v17
	v_rcp_f32_e32 v17, v17
	v_mul_f32_e32 v16, 0xc1000000, v16
	v_mul_f32_e32 v16, v49, v16
	v_mul_f32_e32 v16, 0x3fb8aa3b, v16
	v_exp_f32_e32 v16, v16
	s_nop 0
	v_fma_f32 v18, -v16, v16, 1.0
	v_max_f32_e32 v18, 0, v18
	v_sqrt_f32_e32 v18, v18
	s_nop 0
	v_mul_f32_e32 v17, v17, v18
	ds_write_b32 v46, v16 offset:43648
	v_mul_f32_e32 v17, v154, v17
	v_or_b32_e32 v18, v38, v43
	v_lshl_add_u32 v16, v18, 2, v28
	ds_write_b32 v16, v17
	v_add_f32_e32 v16, v41, v19
	v_mul_f32_e32 v16, 0xbfb8aa3b, v16
	v_exp_f32_e32 v16, v16
	v_add_f32_e32 v17, v40, v23
	v_mul_f32_e32 v17, 0xbfb8aa3b, v17
	v_exp_f32_e32 v17, v17
	v_add_f32_e32 v16, 1.0, v16
	v_rcp_f32_e32 v16, v16
	v_lshlrev_b32_e32 v40, 7, v35
	v_add_f32_e32 v17, 1.0, v17
	v_rcp_f32_e32 v17, v17
	v_mul_f32_e32 v16, 0xc1000000, v16
	v_mul_f32_e32 v16, v49, v16
	v_mul_f32_e32 v16, 0x3fb8aa3b, v16
	v_exp_f32_e32 v16, v16
	v_mov_b32_e32 v41, v105
	v_fma_f32 v18, -v16, v16, 1.0
	v_max_f32_e32 v18, 0, v18
	v_sqrt_f32_e32 v18, v18
	s_nop 0
	v_mul_f32_e32 v17, v17, v18
	ds_write_b32 v44, v16 offset:43648
	v_mul_f32_e32 v17, v155, v17
	v_or_b32_e32 v18, v37, v43
	v_lshl_add_u32 v16, v18, 2, v28
	ds_write_b32 v16, v17
	v_lshl_add_u64 v[16:17], s[2:3], 0, v[40:41]
	v_lshl_add_u64 v[20:21], v[16:17], 0, v[24:25]
	global_load_dwordx4 v[16:19], v[20:21], off
	s_waitcnt vmcnt(0)
	v_mfma_f32_16x16x32_bf16 v[16:19], v[12:15], v[16:19], 0
	global_load_dwordx4 v[20:23], v[20:21], off offset:64
	s_waitcnt vmcnt(0)
	v_mfma_f32_16x16x32_bf16 v[16:19], v[8:11], v[20:23], v[16:19]
	v_lshl_add_u64 v[20:21], s[0:1], 0, v[40:41]
	v_lshl_add_u64 v[24:25], v[20:21], 0, v[24:25]
	global_load_dwordx4 v[20:23], v[24:25], off
	s_waitcnt vmcnt(0)
	v_mfma_f32_16x16x32_bf16 v[12:15], v[12:15], v[20:23], 0
	global_load_dwordx4 v[20:23], v[24:25], off offset:64
	s_waitcnt vmcnt(0)
	v_mfma_f32_16x16x32_bf16 v[8:11], v[8:11], v[20:23], v[12:15]
	s_nop 4
	v_add_f32_e32 v14, v33, v16
	v_mul_f32_e64 v13, |v34|, s14
	v_mul_f32_e32 v14, 0xbfb8aa3b, v14
	v_exp_f32_e32 v13, v13
	v_exp_f32_e32 v14, v14
	v_max_f32_e64 v12, -v34, -v34
	v_max_f32_e32 v12, 0, v12
	v_add_f32_e32 v13, 1.0, v13
	v_add_f32_e32 v14, 1.0, v14
	v_log_f32_e32 v13, v13
	v_rcp_f32_e32 v14, v14
	v_add_f32_e32 v8, v32, v8
	v_mul_f32_e32 v8, 0xbfb8aa3b, v8
	v_fmac_f32_e32 v12, 0x3f317218, v13
	v_mul_f32_e32 v14, 0xc1000000, v14
	v_mul_f32_e32 v14, v12, v14
	v_mul_f32_e32 v14, 0x3fb8aa3b, v14
	v_exp_f32_e32 v14, v14
	v_exp_f32_e32 v8, v8
	v_or_b32_e32 v13, s73, v35
	v_add_f32_e32 v9, v32, v9
	v_fma_f32 v15, -v14, v14, 1.0
	v_add_f32_e32 v8, 1.0, v8
	v_max_f32_e32 v15, 0, v15
	v_rcp_f32_e32 v8, v8
	v_sqrt_f32_e32 v15, v15
	v_mul_f32_e32 v9, 0xbfb8aa3b, v9
	v_exp_f32_e32 v9, v9
	v_mul_f32_e32 v8, v8, v15
	ds_write_b32 v48, v14 offset:43712
	v_add_f32_e32 v9, 1.0, v9
	v_rcp_f32_e32 v9, v9
	v_mul_f32_e32 v8, v156, v8
	v_or_b32_e32 v15, v42, v13
	v_lshl_add_u32 v14, v15, 2, v28
	ds_write_b32 v14, v8
	v_add_f32_e32 v8, v33, v17
	v_mul_f32_e32 v8, 0xbfb8aa3b, v8
	v_exp_f32_e32 v8, v8
	s_nop 0
	v_add_f32_e32 v8, 1.0, v8
	v_rcp_f32_e32 v8, v8
	s_nop 0
	v_mul_f32_e32 v8, 0xc1000000, v8
	v_mul_f32_e32 v8, v12, v8
	v_mul_f32_e32 v8, 0x3fb8aa3b, v8
	v_exp_f32_e32 v8, v8
	s_nop 0
	v_fma_f32 v14, -v8, v8, 1.0
	v_max_f32_e32 v14, 0, v14
	v_sqrt_f32_e32 v14, v14
	s_nop 0
	v_mul_f32_e32 v9, v9, v14
	ds_write_b32 v47, v8 offset:43712
	v_mul_f32_e32 v9, v157, v9
	v_or_b32_e32 v14, v39, v13
	v_lshl_add_u32 v8, v14, 2, v28
	ds_write_b32 v8, v9
	v_add_f32_e32 v8, v33, v18
	v_mul_f32_e32 v8, 0xbfb8aa3b, v8
	v_exp_f32_e32 v8, v8
	v_add_f32_e32 v9, v32, v10
	v_mul_f32_e32 v9, 0xbfb8aa3b, v9
	v_exp_f32_e32 v9, v9
	v_add_f32_e32 v8, 1.0, v8
	v_rcp_f32_e32 v8, v8
	v_add_f32_e32 v9, 1.0, v9
	v_rcp_f32_e32 v9, v9
	v_mul_f32_e32 v8, 0xc1000000, v8
	v_mul_f32_e32 v8, v12, v8
	v_mul_f32_e32 v8, 0x3fb8aa3b, v8
	v_exp_f32_e32 v8, v8
	s_nop 0
	v_fma_f32 v10, -v8, v8, 1.0
	v_max_f32_e32 v10, 0, v10
	v_sqrt_f32_e32 v10, v10
	s_nop 0
	v_mul_f32_e32 v9, v9, v10
	ds_write_b32 v46, v8 offset:43712
	v_mul_f32_e32 v9, v158, v9
	v_or_b32_e32 v10, v38, v13
	v_lshl_add_u32 v8, v10, 2, v28
	ds_write_b32 v8, v9
	v_add_f32_e32 v8, v33, v19
	v_mul_f32_e32 v8, 0xbfb8aa3b, v8
	v_exp_f32_e32 v8, v8
	v_add_f32_e32 v9, v32, v11
	v_mul_f32_e32 v9, 0xbfb8aa3b, v9
	v_exp_f32_e32 v9, v9
	v_add_f32_e32 v8, 1.0, v8
	v_rcp_f32_e32 v8, v8
	v_add_f32_e32 v9, 1.0, v9
	v_rcp_f32_e32 v9, v9
	v_mul_f32_e32 v8, 0xc1000000, v8
	v_mul_f32_e32 v8, v12, v8
	v_mul_f32_e32 v8, 0x3fb8aa3b, v8
	v_exp_f32_e32 v8, v8
	v_ashrrev_i32_e32 v12, 8, v30
	v_fma_f32 v10, -v8, v8, 1.0
	v_max_f32_e32 v10, 0, v10
	v_sqrt_f32_e32 v10, v10
	s_nop 0
	v_mul_f32_e32 v9, v9, v10
	ds_write_b32 v44, v8 offset:43712
	v_mul_f32_e32 v9, v159, v9
	v_or_b32_e32 v10, v37, v13
	v_lshl_add_u32 v8, v10, 2, v28
	ds_write_b32 v8, v9
	v_bfe_u32 v8, v30, 6, 2
	v_lshlrev_b32_e32 v9, 4, v8
	v_xor_b32_e32 v10, 63, v9
	v_cndmask_b32_e32 v25, v10, v9, vcc
	v_lshl_or_b32 v10, v12, 14, v104
	v_lshl_or_b32 v11, v25, 8, v10
	s_waitcnt lgkmcnt(0)
	s_barrier
	v_add_u32_e32 v13, v111, v11
	v_add_u32_e32 v11, v28, v11
	s_cbranch_vccz .Lscan_bwd
	ds_read_b32 v22, v11
	ds_read_b32 v17, v13 offset:43520
	ds_read_b32 v15, v11 offset:256
	ds_read_b32 v161, v13 offset:43776
	ds_read_b32 v16, v11 offset:512
	ds_read_b32 v162, v13 offset:44032
	ds_read_b32 v18, v11 offset:768
	ds_read_b32 v163, v13 offset:44288
	ds_read_b32 v33, v11 offset:1024
	ds_read_b32 v164, v13 offset:44544
	ds_read_b32 v34, v11 offset:1280
	ds_read_b32 v165, v13 offset:44800
	ds_read_b32 v35, v11 offset:1536
	ds_read_b32 v166, v13 offset:45056
	ds_read_b32 v42, v11 offset:1792
	ds_read_b32 v167, v13 offset:45312
	ds_read_b32 v43, v11 offset:2048
	ds_read_b32 v168, v13 offset:45568
	ds_read_b32 v44, v11 offset:2304
	ds_read_b32 v169, v13 offset:45824
	ds_read_b32 v51, v11 offset:2560
	ds_read_b32 v170, v13 offset:46080
	ds_read_b32 v52, v11 offset:2816
	ds_read_b32 v171, v13 offset:46336
	ds_read_b32 v53, v11 offset:3072
	ds_read_b32 v172, v13 offset:46592
	ds_read_b32 v60, v11 offset:3328
	ds_read_b32 v173, v13 offset:46848
	ds_read_b32 v61, v11 offset:3584
	ds_read_b32 v174, v13 offset:47104
	ds_read_b32 v32, v11 offset:3840
	ds_read_b32 v175, v13 offset:47360
	s_branch .Lscan_rd
.Lscan_bwd:
	v_add_u32_e32 v13, 0xfffff100, v13
	v_add_u32_e32 v11, 0xfffff100, v11
	ds_read_b32 v22, v11 offset:3840
	ds_read_b32 v17, v13 offset:47360
	ds_read_b32 v15, v11 offset:3584
	ds_read_b32 v161, v13 offset:47104
	ds_read_b32 v16, v11 offset:3328
	ds_read_b32 v162, v13 offset:46848
	ds_read_b32 v18, v11 offset:3072
	ds_read_b32 v163, v13 offset:46592
	ds_read_b32 v33, v11 offset:2816
	ds_read_b32 v164, v13 offset:46336
	ds_read_b32 v34, v11 offset:2560
	ds_read_b32 v165, v13 offset:46080
	ds_read_b32 v35, v11 offset:2304
	ds_read_b32 v166, v13 offset:45824
	ds_read_b32 v42, v11 offset:2048
	ds_read_b32 v167, v13 offset:45568
	ds_read_b32 v43, v11 offset:1792
	ds_read_b32 v168, v13 offset:45312
	ds_read_b32 v44, v11 offset:1536
	ds_read_b32 v169, v13 offset:45056
	ds_read_b32 v51, v11 offset:1280
	ds_read_b32 v170, v13 offset:44800
	ds_read_b32 v52, v11 offset:1024
	ds_read_b32 v171, v13 offset:44544
	ds_read_b32 v53, v11 offset:768
	ds_read_b32 v172, v13 offset:44288
	ds_read_b32 v60, v11 offset:512
	ds_read_b32 v173, v13 offset:44032
	ds_read_b32 v61, v11 offset:256
	ds_read_b32 v174, v13 offset:43776
	ds_read_b32 v32, v11
	ds_read_b32 v175, v13 offset:43520
.Lscan_rd:
	v_and_b32_e32 v9, 0x3fffff00, v30
	v_lshlrev_b32_e32 v10, 6, v8
	v_cmp_ne_u32_e32 vcc, 0, v8
	v_or3_b32 v9, v10, v9, v31
	s_waitcnt lgkmcnt(0)
	v_fmac_f32_e32 v22, 0, v17
	v_fmac_f32_e32 v15, v22, v161
	v_mul_f32_e32 v13, v17, v161
	v_fmac_f32_e32 v16, v15, v162
	v_mul_f32_e32 v14, v13, v162
	v_fmac_f32_e32 v18, v16, v163
	v_mul_f32_e32 v38, v14, v163
	v_fmac_f32_e32 v33, v18, v164
	v_mul_f32_e32 v23, v38, v164
	v_fmac_f32_e32 v34, v33, v165
	v_mul_f32_e32 v24, v23, v165
	v_fmac_f32_e32 v35, v34, v166
	v_mul_f32_e32 v47, v24, v166
	v_fmac_f32_e32 v42, v35, v167
	v_mul_f32_e32 v40, v47, v167
	v_fmac_f32_e32 v43, v42, v168
	v_mul_f32_e32 v41, v40, v168
	v_fmac_f32_e32 v44, v43, v169
	v_mul_f32_e32 v56, v41, v169
	v_fmac_f32_e32 v51, v44, v170
	v_mul_f32_e32 v49, v56, v170
	v_fmac_f32_e32 v52, v51, v171
	v_mul_f32_e32 v50, v49, v171
	v_fmac_f32_e32 v53, v52, v172
	v_mul_f32_e32 v64, v50, v172
	v_fmac_f32_e32 v60, v53, v173
	v_mul_f32_e32 v58, v64, v173
	v_fmac_f32_e32 v61, v60, v174
	v_mul_f32_e32 v59, v58, v174
	v_fmac_f32_e32 v32, v61, v175
	v_mul_f32_e32 v66, v59, v175
	v_lshlrev_b32_e32 v9, 2, v9
	v_add_u32_e32 v10, v27, v9
	v_add_u32_e32 v9, v29, v9
	ds_write_b32 v10, v66
	ds_write_b32 v9, v32
	s_waitcnt lgkmcnt(0)
	s_barrier
	s_and_saveexec_b64 s[0:1], vcc
	s_cbranch_execz .LBB0_372
	v_lshlrev_b32_e32 v9, 2, v30
	v_and_b32_e32 v9, 0xfffffcfc, v9
	v_add_u32_e32 v10, v29, v9
	v_add_u32_e32 v9, v27, v9
	ds_read_b32 v67, v9
	ds_read_b32 v68, v10
	s_waitcnt lgkmcnt(0)
	v_fmac_f32_e32 v68, 0, v67

.LBB0_376:
	s_or_b64 exec, exec, s[0:1]
	s_add_i32 s17, s17, s36
	v_or_b32_e32 v30, s17, v25
	v_or_b32_e32 v104, s28, v31
	v_ashrrev_i32_e32 v31, 31, v30
	v_lshlrev_b64 v[30:31], 10, v[30:31]
	v_mov_b64_e32 v[8:9], s[8:9]
	v_lshl_add_u64 v[30:31], v[30:31], 0, v[104:105]
	v_mad_i64_i32 v[10:11], s[0:1], v12, s42, v[8:9]
	v_lshlrev_b64 v[30:31], 1, v[30:31]
	v_mov_b64_e32 v[8:9], s[10:11]
	v_readfirstlane_b32 s101, v12
	v_lshl_add_u64 v[222:223], v[10:11], 0, v[30:31]
	v_mad_i64_i32 v[8:9], s[0:1], v12, s42, v[8:9]
	s_cmp_eq_u32 s101, 0
	s_movk_i32 s100, 0x800
	s_cselect_b32 s100, s100, 0xfffff800
	s_cselect_b32 s101, 0, -1
	v_lshl_add_u64 v[224:225], v[8:9], 0, v[30:31]
	v_fmac_f32_e32 v22, v17, v68
	v_mul_f32_e32 v227, v17, v67
	v_bfe_u32 v226, v22, 16, 1
	v_bfe_u32 v228, v227, 16, 1
	v_add3_u32 v226, v22, v226, s25
	v_add3_u32 v228, v227, v228, s25
	global_store_short_d16_hi v[222:223], v226, off
	global_store_short_d16_hi v[224:225], v228, off
	v_lshl_add_u64 v[222:223], v[222:223], 0, s[100:101]
	v_lshl_add_u64 v[224:225], v[224:225], 0, s[100:101]
	v_fmac_f32_e32 v15, v13, v68
	v_mul_f32_e32 v227, v13, v67
	v_bfe_u32 v226, v15, 16, 1
	v_bfe_u32 v228, v227, 16, 1
	v_add3_u32 v226, v15, v226, s25
	v_add3_u32 v228, v227, v228, s25
	global_store_short_d16_hi v[222:223], v226, off
	global_store_short_d16_hi v[224:225], v228, off
	v_lshl_add_u64 v[222:223], v[222:223], 0, s[100:101]
	v_lshl_add_u64 v[224:225], v[224:225], 0, s[100:101]
	v_fmac_f32_e32 v16, v14, v68
	v_mul_f32_e32 v227, v14, v67
	v_bfe_u32 v226, v16, 16, 1
	v_bfe_u32 v228, v227, 16, 1
	v_add3_u32 v226, v16, v226, s25
	v_add3_u32 v228, v227, v228, s25
	global_store_short_d16_hi v[222:223], v226, off
	global_store_short_d16_hi v[224:225], v228, off
	v_lshl_add_u64 v[222:223], v[222:223], 0, s[100:101]
	v_lshl_add_u64 v[224:225], v[224:225], 0, s[100:101]
	v_fmac_f32_e32 v18, v38, v68
	v_mul_f32_e32 v227, v38, v67
	v_bfe_u32 v226, v18, 16, 1
	v_bfe_u32 v228, v227, 16, 1
	v_add3_u32 v226, v18, v226, s25
	v_add3_u32 v228, v227, v228, s25
	global_store_short_d16_hi v[222:223], v226, off
	global_store_short_d16_hi v[224:225], v228, off
	v_lshl_add_u64 v[222:223], v[222:223], 0, s[100:101]
	v_lshl_add_u64 v[224:225], v[224:225], 0, s[100:101]
	v_fmac_f32_e32 v33, v23, v68
	v_mul_f32_e32 v227, v23, v67
	v_bfe_u32 v226, v33, 16, 1
	v_bfe_u32 v228, v227, 16, 1
	v_add3_u32 v226, v33, v226, s25
	v_add3_u32 v228, v227, v228, s25
	global_store_short_d16_hi v[222:223], v226, off
	global_store_short_d16_hi v[224:225], v228, off
	v_lshl_add_u64 v[222:223], v[222:223], 0, s[100:101]
	v_lshl_add_u64 v[224:225], v[224:225], 0, s[100:101]
	v_fmac_f32_e32 v34, v24, v68
	v_mul_f32_e32 v227, v24, v67
	v_bfe_u32 v226, v34, 16, 1
	v_bfe_u32 v228, v227, 16, 1
	v_add3_u32 v226, v34, v226, s25
	v_add3_u32 v228, v227, v228, s25
	global_store_short_d16_hi v[222:223], v226, off
	global_store_short_d16_hi v[224:225], v228, off
	v_lshl_add_u64 v[222:223], v[222:223], 0, s[100:101]
	v_lshl_add_u64 v[224:225], v[224:225], 0, s[100:101]
	v_fmac_f32_e32 v35, v47, v68
	v_mul_f32_e32 v227, v47, v67
	v_bfe_u32 v226, v35, 16, 1
	v_bfe_u32 v228, v227, 16, 1
	v_add3_u32 v226, v35, v226, s25
	v_add3_u32 v228, v227, v228, s25
	global_store_short_d16_hi v[222:223], v226, off
	global_store_short_d16_hi v[224:225], v228, off
	v_lshl_add_u64 v[222:223], v[222:223], 0, s[100:101]
	v_lshl_add_u64 v[224:225], v[224:225], 0, s[100:101]
	v_fmac_f32_e32 v42, v40, v68
	v_mul_f32_e32 v227, v40, v67
	v_bfe_u32 v226, v42, 16, 1
	v_bfe_u32 v228, v227, 16, 1
	v_add3_u32 v226, v42, v226, s25
	v_add3_u32 v228, v227, v228, s25
	global_store_short_d16_hi v[222:223], v226, off
	global_store_short_d16_hi v[224:225], v228, off
	v_lshl_add_u64 v[222:223], v[222:223], 0, s[100:101]
	v_lshl_add_u64 v[224:225], v[224:225], 0, s[100:101]
	v_fmac_f32_e32 v43, v41, v68
	v_mul_f32_e32 v227, v41, v67
	v_bfe_u32 v226, v43, 16, 1
	v_bfe_u32 v228, v227, 16, 1
	v_add3_u32 v226, v43, v226, s25
	v_add3_u32 v228, v227, v228, s25
	global_store_short_d16_hi v[222:223], v226, off
	global_store_short_d16_hi v[224:225], v228, off
	v_lshl_add_u64 v[222:223], v[222:223], 0, s[100:101]
	v_lshl_add_u64 v[224:225], v[224:225], 0, s[100:101]
	v_fmac_f32_e32 v44, v56, v68
	v_mul_f32_e32 v227, v56, v67
	v_bfe_u32 v226, v44, 16, 1
	v_bfe_u32 v228, v227, 16, 1
	v_add3_u32 v226, v44, v226, s25
	v_add3_u32 v228, v227, v228, s25
	global_store_short_d16_hi v[222:223], v226, off
	global_store_short_d16_hi v[224:225], v228, off
	v_lshl_add_u64 v[222:223], v[222:223], 0, s[100:101]
	v_lshl_add_u64 v[224:225], v[224:225], 0, s[100:101]
	v_fmac_f32_e32 v51, v49, v68
	v_mul_f32_e32 v227, v49, v67
	v_bfe_u32 v226, v51, 16, 1
	v_bfe_u32 v228, v227, 16, 1
	v_add3_u32 v226, v51, v226, s25
	v_add3_u32 v228, v227, v228, s25
	global_store_short_d16_hi v[222:223], v226, off
	global_store_short_d16_hi v[224:225], v228, off
	v_lshl_add_u64 v[222:223], v[222:223], 0, s[100:101]
	v_lshl_add_u64 v[224:225], v[224:225], 0, s[100:101]
	v_fmac_f32_e32 v52, v50, v68
	v_mul_f32_e32 v227, v50, v67
	v_bfe_u32 v226, v52, 16, 1
	v_bfe_u32 v228, v227, 16, 1
	v_add3_u32 v226, v52, v226, s25
	v_add3_u32 v228, v227, v228, s25
	global_store_short_d16_hi v[222:223], v226, off
	global_store_short_d16_hi v[224:225], v228, off
	v_lshl_add_u64 v[222:223], v[222:223], 0, s[100:101]
	v_lshl_add_u64 v[224:225], v[224:225], 0, s[100:101]
	v_fmac_f32_e32 v53, v64, v68
	v_mul_f32_e32 v227, v64, v67
	v_bfe_u32 v226, v53, 16, 1
	v_bfe_u32 v228, v227, 16, 1
	v_add3_u32 v226, v53, v226, s25
	v_add3_u32 v228, v227, v228, s25
	global_store_short_d16_hi v[222:223], v226, off
	global_store_short_d16_hi v[224:225], v228, off
	v_lshl_add_u64 v[222:223], v[222:223], 0, s[100:101]
	v_lshl_add_u64 v[224:225], v[224:225], 0, s[100:101]
	v_fmac_f32_e32 v60, v58, v68
	v_mul_f32_e32 v227, v58, v67
	v_bfe_u32 v226, v60, 16, 1
	v_bfe_u32 v228, v227, 16, 1
	v_add3_u32 v226, v60, v226, s25
	v_add3_u32 v228, v227, v228, s25
	global_store_short_d16_hi v[222:223], v226, off
	global_store_short_d16_hi v[224:225], v228, off
	v_lshl_add_u64 v[222:223], v[222:223], 0, s[100:101]
	v_lshl_add_u64 v[224:225], v[224:225], 0, s[100:101]
	v_fmac_f32_e32 v61, v59, v68
	v_mul_f32_e32 v227, v59, v67
	v_bfe_u32 v226, v61, 16, 1
	v_bfe_u32 v228, v227, 16, 1
	v_add3_u32 v226, v61, v226, s25
	v_add3_u32 v228, v227, v228, s25
	global_store_short_d16_hi v[222:223], v226, off
	global_store_short_d16_hi v[224:225], v228, off
	v_lshl_add_u64 v[222:223], v[222:223], 0, s[100:101]
	v_lshl_add_u64 v[224:225], v[224:225], 0, s[100:101]
	v_fmac_f32_e32 v32, v66, v68
	v_mul_f32_e32 v10, v66, v67
	v_bfe_u32 v226, v32, 16, 1
	v_bfe_u32 v228, v10, 16, 1
	v_add3_u32 v226, v32, v226, s25
	v_add3_u32 v228, v10, v228, s25
	global_store_short_d16_hi v[222:223], v226, off
	global_store_short_d16_hi v[224:225], v228, off
	s_and_saveexec_b64 s[0:1], vcc
	s_cbranch_execz .LBB0_359
	v_mul_hi_i32_i24_e32 v9, 0x88, v12
	v_mul_i32_i24_e32 v8, 0x88, v12
	s_ashr_i32 s17, s16, 31
	v_lshl_add_u64 v[8:9], v[8:9], 0, s[16:17]
	v_lshlrev_b64 v[8:9], 12, v[8:9]
	v_lshl_add_u64 v[8:9], s[12:13], 0, v[8:9]
	v_lshlrev_b64 v[14:15], 2, v[104:105]
	v_lshl_add_u64 v[8:9], v[8:9], 0, v[14:15]
	global_store_dword v[8:9], v10, off
	v_add_u32_e32 v10, 2, v12
	v_mov_b64_e32 v[8:9], s[16:17]
	s_movk_i32 s2, 0x88
	v_mad_i64_i32 v[8:9], s[2:3], v10, s2, v[8:9]
	v_lshlrev_b64 v[8:9], 12, v[8:9]
	v_lshl_add_u64 v[8:9], s[12:13], 0, v[8:9]
	v_lshl_add_u64 v[8:9], v[8:9], 0, v[14:15]
	global_store_dword v[8:9], v32, off
	s_branch .LBB0_359
